# in-projection GEMM: tile row/column scales fetched by LDS-DMA at K-loop start, epilogue reads them from LDS
# speedup vs baseline: 1.0023x; 1.0004x over previous
.LBB0_225:
	s_ashr_i32 s43, s42, 31
	s_lshl_b64 s[44:45], s[42:43], 19
	s_add_u32 s44, s12, s44
	s_addc_u32 s45, s13, s45
	s_and_b64 s[46:47], s[40:41], exec
	v_lshl_add_u32 v2, s56, 19, v239
	s_cselect_b32 s43, s45, s11
	s_cselect_b32 s59, s44, s10
	v_add_u32_e32 v245, v2, v238
	v_add_u32_e32 v246, v2, v240
	v_add_u32_e32 v212, v2, v241
	v_add_u32_e32 v214, v2, v242
	s_add_u32 s60, s10, 0x100
	v_mov_b32_e32 v2, 0
	v_mov_b32_e32 v213, v99
	v_mov_b32_e32 v215, v99
	s_addc_u32 s61, s11, 0
	s_mov_b32 s65, -2
	s_mov_b64 s[10:11], 0
	v_mov_b32_e32 v3, v2
	v_mov_b32_e32 v4, v2
	v_mov_b32_e32 v5, v2
	v_mov_b32_e32 v6, v2
	v_mov_b32_e32 v7, v2
	v_mov_b32_e32 v8, v2
	v_mov_b32_e32 v9, v2
	v_mov_b32_e32 v18, v2
	v_mov_b32_e32 v19, v2
	v_mov_b32_e32 v20, v2
	v_mov_b32_e32 v21, v2
	v_mov_b32_e32 v22, v2
	v_mov_b32_e32 v23, v2
	v_mov_b32_e32 v24, v2
	v_mov_b32_e32 v25, v2
	v_mov_b32_e32 v34, v2
	v_mov_b32_e32 v35, v2
	v_mov_b32_e32 v36, v2
	v_mov_b32_e32 v37, v2
	v_mov_b32_e32 v38, v2
	v_mov_b32_e32 v39, v2
	v_mov_b32_e32 v40, v2
	v_mov_b32_e32 v41, v2
	v_mov_b32_e32 v50, v2
	v_mov_b32_e32 v51, v2
	v_mov_b32_e32 v52, v2
	v_mov_b32_e32 v53, v2
	v_mov_b32_e32 v54, v2
	v_mov_b32_e32 v55, v2
	v_mov_b32_e32 v56, v2
	v_mov_b32_e32 v57, v2
	v_mov_b32_e32 v10, v2
	v_mov_b32_e32 v11, v2
	v_mov_b32_e32 v12, v2
	v_mov_b32_e32 v13, v2
	v_mov_b32_e32 v14, v2
	v_mov_b32_e32 v15, v2
	v_mov_b32_e32 v16, v2
	v_mov_b32_e32 v17, v2
	v_mov_b32_e32 v26, v2
	v_mov_b32_e32 v27, v2
	v_mov_b32_e32 v28, v2
	v_mov_b32_e32 v29, v2
	v_mov_b32_e32 v30, v2
	v_mov_b32_e32 v31, v2
	v_mov_b32_e32 v32, v2
	v_mov_b32_e32 v33, v2
	v_mov_b32_e32 v42, v2
	v_mov_b32_e32 v43, v2
	v_mov_b32_e32 v44, v2
	v_mov_b32_e32 v45, v2
	v_mov_b32_e32 v46, v2
	v_mov_b32_e32 v47, v2
	v_mov_b32_e32 v48, v2
	v_mov_b32_e32 v49, v2
	v_mov_b32_e32 v58, v2
	v_mov_b32_e32 v59, v2
	v_mov_b32_e32 v60, v2
	v_mov_b32_e32 v61, v2
	v_mov_b32_e32 v62, v2
	v_mov_b32_e32 v63, v2
	v_mov_b32_e32 v64, v2
	v_mov_b32_e32 v65, v2
	v_mov_b32_e32 v66, v2
	v_mov_b32_e32 v67, v2
	v_mov_b32_e32 v68, v2
	v_mov_b32_e32 v69, v2
	v_mov_b32_e32 v70, v2
	v_mov_b32_e32 v71, v2
	v_mov_b32_e32 v72, v2
	v_mov_b32_e32 v73, v2
	v_mov_b32_e32 v90, v2
	v_mov_b32_e32 v91, v2
	v_mov_b32_e32 v92, v2
	v_mov_b32_e32 v93, v2
	v_mov_b32_e32 v100, v2
	v_mov_b32_e32 v101, v2
	v_mov_b32_e32 v102, v2
	v_mov_b32_e32 v103, v2
	v_mov_b32_e32 v116, v2
	v_mov_b32_e32 v117, v2
	v_mov_b32_e32 v118, v2
	v_mov_b32_e32 v119, v2
	v_mov_b32_e32 v120, v2
	v_mov_b32_e32 v121, v2
	v_mov_b32_e32 v122, v2
	v_mov_b32_e32 v123, v2
	v_mov_b32_e32 v132, v2
	v_mov_b32_e32 v133, v2
	v_mov_b32_e32 v134, v2
	v_mov_b32_e32 v135, v2
	v_mov_b32_e32 v136, v2
	v_mov_b32_e32 v137, v2
	v_mov_b32_e32 v138, v2
	v_mov_b32_e32 v139, v2
	v_mov_b32_e32 v78, v2
	v_mov_b32_e32 v79, v2
	v_mov_b32_e32 v80, v2
	v_mov_b32_e32 v81, v2
	v_mov_b32_e32 v86, v2
	v_mov_b32_e32 v87, v2
	v_mov_b32_e32 v88, v2
	v_mov_b32_e32 v89, v2
	v_mov_b32_e32 v108, v2
	v_mov_b32_e32 v109, v2
	v_mov_b32_e32 v110, v2
	v_mov_b32_e32 v111, v2
	v_mov_b32_e32 v112, v2
	v_mov_b32_e32 v113, v2
	v_mov_b32_e32 v114, v2
	v_mov_b32_e32 v115, v2
	v_mov_b32_e32 v124, v2
	v_mov_b32_e32 v125, v2
	v_mov_b32_e32 v126, v2
	v_mov_b32_e32 v127, v2
	v_mov_b32_e32 v128, v2
	v_mov_b32_e32 v129, v2
	v_mov_b32_e32 v130, v2
	v_mov_b32_e32 v131, v2
	v_mov_b32_e32 v140, v2
	v_mov_b32_e32 v141, v2
	v_mov_b32_e32 v142, v2
	v_mov_b32_e32 v143, v2
	v_mov_b32_e32 v144, v2
	v_mov_b32_e32 v145, v2
	v_mov_b32_e32 v146, v2
	v_mov_b32_e32 v147, v2
	s_waitcnt vmcnt(0)
	v_mbcnt_lo_u32_b32 v3, -1, 0
	v_mbcnt_hi_u32_b32 v3, -1, v3
	v_readfirstlane_b32 s100, v0
	v_lshlrev_b32_e32 v3, 2, v3
	s_lshr_b32 s100, s100, 6
	s_and_b32 vcc_lo, s68, 1
	s_lshl_b32 vcc_lo, vcc_lo, 11
	s_add_i32 vcc_lo, vcc_lo, 0x22400
	s_cmp_gt_u32 s100, 3
	s_cbranch_scc1 .Linpf_cols
	s_lshl_b32 vcc_hi, s100, 8
	s_add_i32 m0, vcc_lo, vcc_hi
	s_lshl_b32 s101, s58, 10
	s_add_i32 s101, s101, vcc_hi
	s_add_u32 s100, s78, s101
	s_addc_u32 s101, s79, 0
	s_branch .Linpf_go
.Linpf_cols:
	s_sub_i32 s100, s100, 4
	s_lshl_b32 vcc_hi, s100, 8
	s_add_i32 m0, vcc_lo, vcc_hi
	s_add_i32 m0, m0, 0x400
	s_lshl_b32 s101, s57, 10
	s_add_i32 s101, s101, vcc_hi
	s_add_u32 s100, s6, s101
	s_addc_u32 s101, s7, 0
.Linpf_go:
	s_nop 0
	global_load_lds_dword v3, s[100:101]
.LBB0_226:
	ds_read_b128 v[148:151], v243
	ds_read_b128 v[152:155], v243 offset:1024
	ds_read_b128 v[156:159], v243 offset:2048
	ds_read_b128 v[160:163], v243 offset:3072
	ds_read_b128 v[74:77], v243 offset:16384
	ds_read_b128 v[82:85], v243 offset:17408
	ds_read_b128 v[94:97], v243 offset:18432
	ds_read_b128 v[104:107], v243 offset:19456
	s_cmp_eq_u32 s65, 12
	s_cselect_b64 s[48:49], -1, 0
	s_add_i32 m0, s17, 0xc000
	s_add_u32 s46, s34, s10
	s_addc_u32 s47, s35, s11
	ds_read_b128 v[188:191], v244
	ds_read_b128 v[192:195], v244 offset:1024
	ds_read_b128 v[180:183], v244 offset:2048
	ds_read_b128 v[184:187], v244 offset:3072
	ds_read_b128 v[172:175], v244 offset:4096
	ds_read_b128 v[176:179], v244 offset:5120
	ds_read_b128 v[164:167], v244 offset:6144
	ds_read_b128 v[168:171], v244 offset:7168
	global_load_lds_dwordx4 v208, s[46:47]
	s_add_i32 m0, s17, 0xe000
	s_nop 0
	global_load_lds_dwordx4 v210, s[46:47]
	s_and_b64 s[46:47], s[40:41], s[48:49]
	s_andn2_b64 vcc, exec, s[46:47]
	s_cbranch_vccnz .LBB0_228
	v_mov_b64_e32 v[216:217], v[214:215]
	v_mov_b64_e32 v[218:219], v[212:213]
	v_mov_b32_e32 v206, v246
	v_mov_b32_e32 v98, v245
	v_mov_b32_e32 v210, v214
	v_mov_b32_e32 v208, v212
	s_branch .LBB0_229

.LBB0_233:
	s_lshl_b32 s10, s58, 8
	s_lshl_b32 s11, s57, 8
	v_mov_b32_e32 v74, v201
	v_mov_b32_e32 v148, v237
	s_add_i32 s10, s10, s29
	s_or_b32 s11, s11, s2
	v_cvt_f32_i32_e32 v145, v145
	v_lshl_add_u32 v154, v74, 3, s11
	v_add_u32_e32 v166, s10, v148
	v_ashrrev_i32_e32 v155, 31, v154
	v_ashrrev_i32_e32 v167, 31, v166
	s_and_b32 s100, s68, 1
	s_lshl_b32 s100, s100, 11
	s_add_i32 s100, s100, 0x22400
	s_lshl_b32 s101, s29, 2
	s_add_i32 s101, s101, s100
	v_lshl_add_u32 v152, v148, 2, s101
	s_lshl_b32 s101, s2, 2
	s_add_i32 s101, s101, s100
	s_add_i32 s101, s101, 0x400
	v_lshl_add_u32 v82, v74, 5, s101
	ds_read_b128 v[94:97], v82 offset:16
	ds_read_b128 v[104:107], v82
	ds_read_b128 v[74:77], v82 offset:528
	ds_read_b128 v[82:85], v82 offset:512
	ds_read_b32 v148, v152 offset:704
	ds_read_b32 v150, v152 offset:640
	ds_read_b32 v156, v152 offset:576
	ds_read_b32 v158, v152 offset:512
	ds_read_b32 v160, v152 offset:192
	ds_read_b32 v162, v152 offset:128
	ds_read_b32 v164, v152 offset:64
	ds_read_b32 v168, v152
	v_cvt_f32_i32_e32 v144, v144
	v_cvt_f32_i32_e32 v147, v147
	v_cvt_f32_i32_e32 v146, v146
	v_cvt_f32_i32_e32 v141, v141
	v_cvt_f32_i32_e32 v140, v140
	v_cvt_f32_i32_e32 v143, v143
	v_cvt_f32_i32_e32 v142, v142
	v_cvt_f32_i32_e32 v137, v137
	v_cvt_f32_i32_e32 v136, v136
	v_cvt_f32_i32_e32 v139, v139
	v_cvt_f32_i32_e32 v138, v138
	v_cvt_f32_i32_e32 v133, v133
	v_cvt_f32_i32_e32 v132, v132
	v_cvt_f32_i32_e32 v135, v135
	v_cvt_f32_i32_e32 v134, v134
	v_mov_b64_e32 v[152:153], s[94:95]
	v_cvt_f32_i32_e32 v129, v129
	v_cvt_f32_i32_e32 v128, v128
	v_cvt_f32_i32_e32 v131, v131
	v_cvt_f32_i32_e32 v130, v130
	v_cvt_f32_i32_e32 v125, v125
	v_cvt_f32_i32_e32 v124, v124
	v_cvt_f32_i32_e32 v127, v127
	v_cvt_f32_i32_e32 v126, v126
	v_add_u32_e32 v165, 16, v166
	v_add_u32_e32 v163, 32, v166
	v_add_u32_e32 v161, 48, v166
	v_add_u32_e32 v159, 0x80, v166
	v_add_u32_e32 v157, 0x90, v166
	v_add_u32_e32 v151, 0xa0, v166
	v_add_u32_e32 v149, 0xb0, v166
	v_mad_i64_i32 v[166:167], s[10:11], v166, s30, v[152:153]
	v_lshlrev_b64 v[154:155], 1, v[154:155]
	v_cvt_f32_i32_e32 v121, v121
	v_cvt_f32_i32_e32 v120, v120
	v_cvt_f32_i32_e32 v123, v123
	v_cvt_f32_i32_e32 v122, v122
	v_cvt_f32_i32_e32 v117, v117
	v_cvt_f32_i32_e32 v116, v116
	v_cvt_f32_i32_e32 v119, v119
	v_cvt_f32_i32_e32 v118, v118
	v_lshl_add_u64 v[166:167], v[166:167], 0, v[154:155]
	v_cvt_f32_i32_e32 v113, v113
	v_cvt_f32_i32_e32 v112, v112
	v_cvt_f32_i32_e32 v115, v115
	v_cvt_f32_i32_e32 v114, v114
	v_cvt_f32_i32_e32 v109, v109
	v_cvt_f32_i32_e32 v108, v108
	v_cvt_f32_i32_e32 v111, v111
	v_cvt_f32_i32_e32 v110, v110
	v_cvt_f32_i32_e32 v101, v101
	v_cvt_f32_i32_e32 v100, v100
	v_cvt_f32_i32_e32 v103, v103
	v_cvt_f32_i32_e32 v102, v102
	v_cvt_f32_i32_e32 v91, v91
	v_cvt_f32_i32_e32 v90, v90
	v_cvt_f32_i32_e32 v93, v93
	v_cvt_f32_i32_e32 v92, v92
	v_cvt_f32_i32_e32 v87, v87
	v_cvt_f32_i32_e32 v86, v86
	v_cvt_f32_i32_e32 v89, v89
	v_cvt_f32_i32_e32 v88, v88
	v_cvt_f32_i32_e32 v79, v79
	v_cvt_f32_i32_e32 v78, v78
	v_cvt_f32_i32_e32 v81, v81
	v_cvt_f32_i32_e32 v80, v80
	v_cvt_f32_i32_e32 v71, v71
	v_cvt_f32_i32_e32 v70, v70
	s_waitcnt lgkmcnt(0)
	v_pk_mul_f32 v[146:147], v[106:107], v[146:147]
	v_pk_mul_f32 v[144:145], v[104:105], v[144:145]
	v_pk_mul_f32 v[142:143], v[96:97], v[142:143]
	v_pk_mul_f32 v[140:141], v[94:95], v[140:141]
	v_pk_mul_f32 v[146:147], v[146:147], v[168:169] op_sel_hi:[1,0]
	v_pk_mul_f32 v[144:145], v[144:145], v[168:169] op_sel_hi:[1,0]
	v_pk_mul_f32 v[170:171], v[142:143], v[168:169] op_sel_hi:[1,0]
	v_pk_mul_f32 v[142:143], v[140:141], v[168:169] op_sel_hi:[1,0]
	v_cvt_pk_bf16_f32 v140, v144, v145
	v_cvt_pk_bf16_f32 v141, v146, v147
	v_pk_mul_f32 v[138:139], v[84:85], v[138:139]
	v_pk_mul_f32 v[136:137], v[82:83], v[136:137]
	v_pk_mul_f32 v[134:135], v[76:77], v[134:135]
	v_pk_mul_f32 v[132:133], v[74:75], v[132:133]
	v_cvt_pk_bf16_f32 v142, v142, v143
	v_cvt_pk_bf16_f32 v143, v170, v171
	global_store_dwordx4 v[166:167], v[140:143], off
	v_pk_mul_f32 v[138:139], v[138:139], v[168:169] op_sel_hi:[1,0]
	v_pk_mul_f32 v[136:137], v[136:137], v[168:169] op_sel_hi:[1,0]
	v_pk_mul_f32 v[140:141], v[134:135], v[168:169] op_sel_hi:[1,0]
	v_pk_mul_f32 v[134:135], v[132:133], v[168:169] op_sel_hi:[1,0]
	v_cvt_pk_bf16_f32 v132, v136, v137
	v_cvt_pk_bf16_f32 v133, v138, v139
	v_pk_mul_f32 v[130:131], v[106:107], v[130:131]
	v_cvt_pk_bf16_f32 v134, v134, v135
	v_cvt_pk_bf16_f32 v135, v140, v141
	global_store_dwordx4 v[166:167], v[132:135], off offset:256
	v_pk_mul_f32 v[128:129], v[104:105], v[128:129]
	v_pk_mul_f32 v[126:127], v[96:97], v[126:127]
	v_mad_i64_i32 v[132:133], s[10:11], v165, s30, v[152:153]
	v_pk_mul_f32 v[124:125], v[94:95], v[124:125]
	v_lshl_add_u64 v[132:133], v[132:133], 0, v[154:155]
	v_pk_mul_f32 v[130:131], v[130:131], v[164:165] op_sel_hi:[1,0]
	v_pk_mul_f32 v[128:129], v[128:129], v[164:165] op_sel_hi:[1,0]
	v_pk_mul_f32 v[134:135], v[126:127], v[164:165] op_sel_hi:[1,0]
	v_pk_mul_f32 v[126:127], v[124:125], v[164:165] op_sel_hi:[1,0]
	v_cvt_pk_bf16_f32 v124, v128, v129
	v_cvt_pk_bf16_f32 v125, v130, v131
	v_pk_mul_f32 v[122:123], v[84:85], v[122:123]
	v_pk_mul_f32 v[120:121], v[82:83], v[120:121]
	v_pk_mul_f32 v[118:119], v[76:77], v[118:119]
	v_pk_mul_f32 v[116:117], v[74:75], v[116:117]
	v_cvt_pk_bf16_f32 v126, v126, v127
	v_cvt_pk_bf16_f32 v127, v134, v135
	global_store_dwordx4 v[132:133], v[124:127], off
	v_pk_mul_f32 v[122:123], v[122:123], v[164:165] op_sel_hi:[1,0]
	v_pk_mul_f32 v[120:121], v[120:121], v[164:165] op_sel_hi:[1,0]
	v_pk_mul_f32 v[124:125], v[118:119], v[164:165] op_sel_hi:[1,0]
	v_pk_mul_f32 v[118:119], v[116:117], v[164:165] op_sel_hi:[1,0]
	v_cvt_pk_bf16_f32 v116, v120, v121
	v_cvt_pk_bf16_f32 v117, v122, v123
	v_pk_mul_f32 v[114:115], v[106:107], v[114:115]
	v_cvt_pk_bf16_f32 v118, v118, v119
	v_cvt_pk_bf16_f32 v119, v124, v125
	global_store_dwordx4 v[132:133], v[116:119], off offset:256
	v_pk_mul_f32 v[112:113], v[104:105], v[112:113]
	v_pk_mul_f32 v[110:111], v[96:97], v[110:111]
	v_mad_i64_i32 v[116:117], s[10:11], v163, s30, v[152:153]
	v_pk_mul_f32 v[108:109], v[94:95], v[108:109]
	v_cvt_f32_i32_e32 v73, v73
	v_cvt_f32_i32_e32 v72, v72
	v_cvt_f32_i32_e32 v67, v67
	v_cvt_f32_i32_e32 v66, v66
	v_cvt_f32_i32_e32 v69, v69
	v_cvt_f32_i32_e32 v68, v68
	v_lshl_add_u64 v[116:117], v[116:117], 0, v[154:155]
	v_pk_mul_f32 v[114:115], v[114:115], v[162:163] op_sel_hi:[1,0]
	v_pk_mul_f32 v[112:113], v[112:113], v[162:163] op_sel_hi:[1,0]
	v_pk_mul_f32 v[118:119], v[110:111], v[162:163] op_sel_hi:[1,0]
	v_pk_mul_f32 v[110:111], v[108:109], v[162:163] op_sel_hi:[1,0]
	v_cvt_pk_bf16_f32 v108, v112, v113
	v_cvt_pk_bf16_f32 v109, v114, v115
	v_pk_mul_f32 v[102:103], v[84:85], v[102:103]
	v_pk_mul_f32 v[100:101], v[82:83], v[100:101]
	v_pk_mul_f32 v[92:93], v[76:77], v[92:93]
	v_pk_mul_f32 v[90:91], v[74:75], v[90:91]
	v_cvt_pk_bf16_f32 v110, v110, v111
	v_cvt_pk_bf16_f32 v111, v118, v119
	global_store_dwordx4 v[116:117], v[108:111], off
	v_pk_mul_f32 v[102:103], v[102:103], v[162:163] op_sel_hi:[1,0]
	v_pk_mul_f32 v[100:101], v[100:101], v[162:163] op_sel_hi:[1,0]
	v_pk_mul_f32 v[108:109], v[92:93], v[162:163] op_sel_hi:[1,0]
	v_pk_mul_f32 v[92:93], v[90:91], v[162:163] op_sel_hi:[1,0]
	v_cvt_pk_bf16_f32 v90, v100, v101
	v_cvt_pk_bf16_f32 v91, v102, v103
	v_cvt_f32_i32_e32 v63, v63
	v_cvt_f32_i32_e32 v62, v62
	v_cvt_f32_i32_e32 v65, v65
	v_cvt_f32_i32_e32 v64, v64
	v_cvt_f32_i32_e32 v59, v59
	v_cvt_f32_i32_e32 v58, v58
	v_cvt_f32_i32_e32 v61, v61
	v_cvt_f32_i32_e32 v60, v60
	v_cvt_pk_bf16_f32 v92, v92, v93
	v_cvt_pk_bf16_f32 v93, v108, v109
	global_store_dwordx4 v[116:117], v[90:93], off offset:256
	v_pk_mul_f32 v[88:89], v[106:107], v[88:89]
	v_pk_mul_f32 v[86:87], v[104:105], v[86:87]
	v_mad_i64_i32 v[90:91], s[10:11], v161, s30, v[152:153]
	v_pk_mul_f32 v[80:81], v[96:97], v[80:81]
	v_pk_mul_f32 v[78:79], v[94:95], v[78:79]
	v_cvt_f32_i32_e32 v55, v55
	v_cvt_f32_i32_e32 v54, v54
	v_cvt_f32_i32_e32 v57, v57
	v_cvt_f32_i32_e32 v56, v56
	v_cvt_f32_i32_e32 v51, v51
	v_cvt_f32_i32_e32 v50, v50
	v_cvt_f32_i32_e32 v53, v53
	v_cvt_f32_i32_e32 v52, v52
	v_lshl_add_u64 v[90:91], v[90:91], 0, v[154:155]
	v_pk_mul_f32 v[88:89], v[88:89], v[160:161] op_sel_hi:[1,0]
	v_pk_mul_f32 v[86:87], v[86:87], v[160:161] op_sel_hi:[1,0]
	v_pk_mul_f32 v[92:93], v[80:81], v[160:161] op_sel_hi:[1,0]
	v_pk_mul_f32 v[80:81], v[78:79], v[160:161] op_sel_hi:[1,0]
	v_cvt_pk_bf16_f32 v78, v86, v87
	v_cvt_pk_bf16_f32 v79, v88, v89
	v_pk_mul_f32 v[72:73], v[84:85], v[72:73]
	v_pk_mul_f32 v[70:71], v[82:83], v[70:71]
	v_pk_mul_f32 v[68:69], v[76:77], v[68:69]
	v_pk_mul_f32 v[66:67], v[74:75], v[66:67]
	v_cvt_pk_bf16_f32 v80, v80, v81
	v_cvt_pk_bf16_f32 v81, v92, v93
	global_store_dwordx4 v[90:91], v[78:81], off
	v_pk_mul_f32 v[72:73], v[72:73], v[160:161] op_sel_hi:[1,0]
	v_pk_mul_f32 v[70:71], v[70:71], v[160:161] op_sel_hi:[1,0]
	v_pk_mul_f32 v[78:79], v[68:69], v[160:161] op_sel_hi:[1,0]
	v_pk_mul_f32 v[68:69], v[66:67], v[160:161] op_sel_hi:[1,0]
	v_cvt_pk_bf16_f32 v66, v70, v71
	v_cvt_pk_bf16_f32 v67, v72, v73
	v_cvt_f32_i32_e32 v47, v47
	v_cvt_f32_i32_e32 v46, v46
	v_cvt_f32_i32_e32 v49, v49
	v_cvt_f32_i32_e32 v48, v48
	v_cvt_f32_i32_e32 v43, v43
	v_cvt_f32_i32_e32 v42, v42
	v_cvt_f32_i32_e32 v45, v45
	v_cvt_f32_i32_e32 v44, v44
	v_cvt_pk_bf16_f32 v68, v68, v69
	v_cvt_pk_bf16_f32 v69, v78, v79
	global_store_dwordx4 v[90:91], v[66:69], off offset:256
	v_pk_mul_f32 v[64:65], v[106:107], v[64:65]
	v_pk_mul_f32 v[62:63], v[104:105], v[62:63]
	v_mad_i64_i32 v[66:67], s[10:11], v159, s30, v[152:153]
	v_pk_mul_f32 v[60:61], v[96:97], v[60:61]
	v_pk_mul_f32 v[58:59], v[94:95], v[58:59]
	v_cvt_f32_i32_e32 v39, v39
	v_cvt_f32_i32_e32 v38, v38
	v_cvt_f32_i32_e32 v41, v41
	v_cvt_f32_i32_e32 v40, v40
	v_cvt_f32_i32_e32 v35, v35
	v_cvt_f32_i32_e32 v34, v34
	v_cvt_f32_i32_e32 v37, v37
	v_cvt_f32_i32_e32 v36, v36
	v_lshl_add_u64 v[66:67], v[66:67], 0, v[154:155]
	v_pk_mul_f32 v[64:65], v[64:65], v[158:159] op_sel_hi:[1,0]
	v_pk_mul_f32 v[62:63], v[62:63], v[158:159] op_sel_hi:[1,0]
	v_pk_mul_f32 v[68:69], v[60:61], v[158:159] op_sel_hi:[1,0]
	v_pk_mul_f32 v[60:61], v[58:59], v[158:159] op_sel_hi:[1,0]
	v_cvt_pk_bf16_f32 v58, v62, v63
	v_cvt_pk_bf16_f32 v59, v64, v65
	v_pk_mul_f32 v[56:57], v[84:85], v[56:57]
	v_pk_mul_f32 v[54:55], v[82:83], v[54:55]
	v_pk_mul_f32 v[52:53], v[76:77], v[52:53]
	v_pk_mul_f32 v[50:51], v[74:75], v[50:51]
	v_cvt_pk_bf16_f32 v60, v60, v61
	v_cvt_pk_bf16_f32 v61, v68, v69
	global_store_dwordx4 v[66:67], v[58:61], off
	v_pk_mul_f32 v[56:57], v[56:57], v[158:159] op_sel_hi:[1,0]
	v_pk_mul_f32 v[54:55], v[54:55], v[158:159] op_sel_hi:[1,0]
	v_pk_mul_f32 v[58:59], v[52:53], v[158:159] op_sel_hi:[1,0]
	v_pk_mul_f32 v[52:53], v[50:51], v[158:159] op_sel_hi:[1,0]
	v_cvt_pk_bf16_f32 v50, v54, v55
	v_cvt_pk_bf16_f32 v51, v56, v57
	v_cvt_f32_i32_e32 v31, v31
	v_cvt_f32_i32_e32 v30, v30
	v_cvt_f32_i32_e32 v33, v33
	v_cvt_f32_i32_e32 v32, v32
	v_cvt_f32_i32_e32 v27, v27
	v_cvt_f32_i32_e32 v26, v26
	v_cvt_f32_i32_e32 v29, v29
	v_cvt_f32_i32_e32 v28, v28
	v_cvt_pk_bf16_f32 v52, v52, v53
	v_cvt_pk_bf16_f32 v53, v58, v59
	global_store_dwordx4 v[66:67], v[50:53], off offset:256
	v_pk_mul_f32 v[48:49], v[106:107], v[48:49]
	v_pk_mul_f32 v[46:47], v[104:105], v[46:47]
	v_mad_i64_i32 v[50:51], s[10:11], v157, s30, v[152:153]
	v_pk_mul_f32 v[44:45], v[96:97], v[44:45]
	v_pk_mul_f32 v[42:43], v[94:95], v[42:43]
	v_cvt_f32_i32_e32 v23, v23
	v_cvt_f32_i32_e32 v22, v22
	v_cvt_f32_i32_e32 v25, v25
	v_cvt_f32_i32_e32 v24, v24
	v_cvt_f32_i32_e32 v19, v19
	v_cvt_f32_i32_e32 v18, v18
	v_cvt_f32_i32_e32 v21, v21
	v_cvt_f32_i32_e32 v20, v20
	v_lshl_add_u64 v[50:51], v[50:51], 0, v[154:155]
	v_pk_mul_f32 v[48:49], v[48:49], v[156:157] op_sel_hi:[1,0]
	v_pk_mul_f32 v[46:47], v[46:47], v[156:157] op_sel_hi:[1,0]
	v_pk_mul_f32 v[52:53], v[44:45], v[156:157] op_sel_hi:[1,0]
	v_pk_mul_f32 v[44:45], v[42:43], v[156:157] op_sel_hi:[1,0]
	v_cvt_pk_bf16_f32 v42, v46, v47
	v_cvt_pk_bf16_f32 v43, v48, v49
	v_pk_mul_f32 v[40:41], v[84:85], v[40:41]
	v_pk_mul_f32 v[38:39], v[82:83], v[38:39]
	v_pk_mul_f32 v[36:37], v[76:77], v[36:37]
	v_pk_mul_f32 v[34:35], v[74:75], v[34:35]
	v_cvt_pk_bf16_f32 v44, v44, v45
	v_cvt_pk_bf16_f32 v45, v52, v53
	global_store_dwordx4 v[50:51], v[42:45], off
	v_pk_mul_f32 v[40:41], v[40:41], v[156:157] op_sel_hi:[1,0]
	v_pk_mul_f32 v[38:39], v[38:39], v[156:157] op_sel_hi:[1,0]
	v_pk_mul_f32 v[42:43], v[36:37], v[156:157] op_sel_hi:[1,0]
	v_pk_mul_f32 v[36:37], v[34:35], v[156:157] op_sel_hi:[1,0]
	v_cvt_pk_bf16_f32 v34, v38, v39
	v_cvt_pk_bf16_f32 v35, v40, v41
	v_cvt_f32_i32_e32 v15, v15
	v_cvt_f32_i32_e32 v14, v14
	v_cvt_f32_i32_e32 v17, v17
	v_cvt_f32_i32_e32 v16, v16
	v_cvt_f32_i32_e32 v11, v11
	v_cvt_f32_i32_e32 v10, v10
	v_cvt_f32_i32_e32 v13, v13
	v_cvt_f32_i32_e32 v12, v12
	v_cvt_pk_bf16_f32 v36, v36, v37
	v_cvt_pk_bf16_f32 v37, v42, v43
	global_store_dwordx4 v[50:51], v[34:37], off offset:256
	v_pk_mul_f32 v[32:33], v[106:107], v[32:33]
	v_pk_mul_f32 v[30:31], v[104:105], v[30:31]
	v_mad_i64_i32 v[34:35], s[10:11], v151, s30, v[152:153]
	v_pk_mul_f32 v[28:29], v[96:97], v[28:29]
	v_pk_mul_f32 v[26:27], v[94:95], v[26:27]
	v_cvt_f32_i32_e32 v3, v3
	v_cvt_f32_i32_e32 v2, v2
	v_cvt_f32_i32_e32 v5, v5
	v_cvt_f32_i32_e32 v4, v4
	v_lshl_add_u64 v[34:35], v[34:35], 0, v[154:155]
	v_pk_mul_f32 v[32:33], v[32:33], v[150:151] op_sel_hi:[1,0]
	v_pk_mul_f32 v[30:31], v[30:31], v[150:151] op_sel_hi:[1,0]
	v_pk_mul_f32 v[36:37], v[28:29], v[150:151] op_sel_hi:[1,0]
	v_pk_mul_f32 v[28:29], v[26:27], v[150:151] op_sel_hi:[1,0]
	v_cvt_pk_bf16_f32 v26, v30, v31
	v_cvt_pk_bf16_f32 v27, v32, v33
	v_pk_mul_f32 v[24:25], v[84:85], v[24:25]
	v_pk_mul_f32 v[22:23], v[82:83], v[22:23]
	v_pk_mul_f32 v[20:21], v[76:77], v[20:21]
	v_pk_mul_f32 v[18:19], v[74:75], v[18:19]
	v_cvt_f32_i32_e32 v7, v7
	v_cvt_f32_i32_e32 v6, v6
	v_cvt_f32_i32_e32 v9, v9
	v_cvt_f32_i32_e32 v8, v8
	v_cvt_pk_bf16_f32 v28, v28, v29
	v_cvt_pk_bf16_f32 v29, v36, v37
	global_store_dwordx4 v[34:35], v[26:29], off
	v_pk_mul_f32 v[24:25], v[24:25], v[150:151] op_sel_hi:[1,0]
	v_pk_mul_f32 v[22:23], v[22:23], v[150:151] op_sel_hi:[1,0]
	v_pk_mul_f32 v[26:27], v[20:21], v[150:151] op_sel_hi:[1,0]
	v_pk_mul_f32 v[20:21], v[18:19], v[150:151] op_sel_hi:[1,0]
	v_cvt_pk_bf16_f32 v18, v22, v23
	v_cvt_pk_bf16_f32 v19, v24, v25
	v_pk_mul_f32 v[16:17], v[106:107], v[16:17]
	v_cvt_pk_bf16_f32 v20, v20, v21
	v_cvt_pk_bf16_f32 v21, v26, v27
	global_store_dwordx4 v[34:35], v[18:21], off offset:256
	v_pk_mul_f32 v[14:15], v[104:105], v[14:15]
	v_pk_mul_f32 v[12:13], v[96:97], v[12:13]
	v_mad_i64_i32 v[18:19], s[10:11], v149, s30, v[152:153]
	v_pk_mul_f32 v[10:11], v[94:95], v[10:11]
	v_lshl_add_u64 v[18:19], v[18:19], 0, v[154:155]
	v_pk_mul_f32 v[16:17], v[16:17], v[148:149] op_sel_hi:[1,0]
	v_pk_mul_f32 v[14:15], v[14:15], v[148:149] op_sel_hi:[1,0]
	v_pk_mul_f32 v[20:21], v[12:13], v[148:149] op_sel_hi:[1,0]
	v_pk_mul_f32 v[12:13], v[10:11], v[148:149] op_sel_hi:[1,0]
	v_cvt_pk_bf16_f32 v10, v14, v15
	v_cvt_pk_bf16_f32 v11, v16, v17
	v_pk_mul_f32 v[4:5], v[76:77], v[4:5]
	v_pk_mul_f32 v[2:3], v[74:75], v[2:3]
	v_cvt_pk_bf16_f32 v12, v12, v13
	v_cvt_pk_bf16_f32 v13, v20, v21
	global_store_dwordx4 v[18:19], v[10:13], off
	v_pk_mul_f32 v[8:9], v[84:85], v[8:9]
	v_pk_mul_f32 v[6:7], v[82:83], v[6:7]
	v_pk_mul_f32 v[10:11], v[4:5], v[148:149] op_sel_hi:[1,0]
	v_pk_mul_f32 v[4:5], v[2:3], v[148:149] op_sel_hi:[1,0]
	s_mov_b64 s[10:11], -1
	s_andn2_b64 vcc, exec, s[40:41]
	v_readlane_b32 s60, v254, 61
	v_readlane_b32 s59, v254, 62
	s_mov_b64 s[46:47], s[36:37]
	v_readlane_b32 s65, v255, 3
	v_pk_mul_f32 v[8:9], v[8:9], v[148:149] op_sel_hi:[1,0]
	v_pk_mul_f32 v[6:7], v[6:7], v[148:149] op_sel_hi:[1,0]
	s_nop 0
	v_cvt_pk_bf16_f32 v2, v6, v7
	v_cvt_pk_bf16_f32 v3, v8, v9
	v_cvt_pk_bf16_f32 v4, v4, v5
	v_cvt_pk_bf16_f32 v5, v10, v11
	global_store_dwordx4 v[18:19], v[2:5], off offset:256
	s_cbranch_vccnz .LBB0_222
	s_andn2_b64 vcc, exec, s[4:5]
	s_cbranch_vccnz .LBB0_221
	s_barrier
	s_branch .LBB0_221
